# gcn layer 1: gather-loop address arithmetic trimmed (one hoisted base, ds_read2_b64 for the two middle CSR entries)
# speedup vs baseline: 1.0005x; 1.0005x over previous
.LBB4_22:
	v_mbcnt_hi_u32_b32 v8, -1, v37
	v_and_b32_e32 v2, 64, v8
	v_add_u32_e32 v20, 64, v2
	v_xor_b32_e32 v2, 4, v8
	v_cmp_lt_i32_e32 vcc, v2, v20
	v_mov_b32_e32 v3, 0
	s_waitcnt vmcnt(0) lgkmcnt(1)
	v_fma_mix_f32 v3, v10, v14, v3 op_sel:[1,0,0] op_sel_hi:[1,0,0]
	v_mov_b32_e32 v5, 0
	v_cndmask_b32_e32 v2, v8, v2, vcc
	v_lshlrev_b32_e32 v2, 2, v2
	s_waitcnt lgkmcnt(0)
	ds_bpermute_b32 v4, v2, v36
	v_mov_b32_e32 v2, 0
	v_fma_mix_f32 v2, v10, v14, v2 op_sel:[0,0,0] op_sel_hi:[1,0,0]
	v_fma_mix_f32 v5, v11, v14, v5 op_sel:[1,0,0] op_sel_hi:[1,0,0]
	v_mov_b32_e32 v9, 0
	s_waitcnt lgkmcnt(0)
	v_max_i32_e32 v6, v36, v4
	v_xor_b32_e32 v4, 8, v8
	v_cmp_lt_i32_e32 vcc, v4, v20
	v_mov_b32_e32 v38, v14
	v_fma_mix_f32 v9, v13, v14, v9 op_sel:[1,0,0] op_sel_hi:[1,0,0]
	s_nop 0
	v_cndmask_b32_e32 v4, v8, v4, vcc
	v_lshlrev_b32_e32 v4, 2, v4
	ds_bpermute_b32 v7, v4, v6
	v_mov_b32_e32 v4, 0
	v_fma_mix_f32 v4, v11, v14, v4 op_sel:[0,0,0] op_sel_hi:[1,0,0]
	v_xor_b32_e32 v11, 32, v8
	s_waitcnt lgkmcnt(0)
	v_max_i32_e32 v10, v6, v7
	v_xor_b32_e32 v6, 16, v8
	v_cmp_lt_i32_e32 vcc, v6, v20
	v_mov_b32_e32 v7, 0
	v_fma_mix_f32 v7, v12, v14, v7 op_sel:[1,0,0] op_sel_hi:[1,0,0]
	s_nop 0
	v_cndmask_b32_e32 v6, v8, v6, vcc
	v_lshlrev_b32_e32 v32, 2, v6
	ds_bpermute_b32 v21, v32, v10
	v_cmp_lt_i32_e32 vcc, v11, v20
	v_mov_b32_e32 v6, 0
	v_fma_mix_f32 v6, v12, v14, v6 op_sel:[0,0,0] op_sel_hi:[1,0,0]
	s_waitcnt lgkmcnt(0)
	v_max_i32_e32 v10, v10, v21
	v_cndmask_b32_e32 v8, v8, v11, vcc
	v_lshlrev_b32_e32 v33, 2, v8
	ds_bpermute_b32 v11, v33, v10
	v_mov_b32_e32 v8, 0
	v_fma_mix_f32 v8, v13, v14, v8 op_sel:[0,0,0] op_sel_hi:[1,0,0]
	s_waitcnt lgkmcnt(0)
	v_max_i32_e32 v10, v10, v11
	v_cmp_lt_i32_e32 vcc, 0, v10
	s_and_saveexec_b64 s[22:23], vcc
	s_cbranch_execz .LBB4_26
	v_sub_u32_e32 v11, v15, v18
	v_lshlrev_b32_e32 v11, 3, v11
	v_add_u32_e32 v11, 0x4400, v11
	s_mov_b32 s26, 0
	s_mov_b64 s[24:25], 0
	v_mov_b32_e32 v38, v14
.LBB4_24:
	s_lshl_b32 s0, s26, 3
	v_add_u32_e32 v20, s0, v11
	ds_read_b64 v[12:13], v20
	ds_read2_b64 v[44:47], v20 offset0:1 offset1:2
	ds_read_b64 v[48:49], v20 offset:24
	v_cmp_lt_i32_e32 vcc, s26, v36
	s_add_i32 s0, s26, 1
	s_add_i32 s4, s26, 2
	s_waitcnt lgkmcnt(2)
	v_cndmask_b32_e32 v12, v16, v12, vcc
	v_cmp_lt_i32_e64 s[0:1], s0, v36
	v_cmp_lt_i32_e64 s[4:5], s4, v36
	s_add_i32 s6, s26, 3
	s_waitcnt lgkmcnt(1)
	v_cndmask_b32_e64 v15, v16, v44, s[0:1]
	s_waitcnt lgkmcnt(1)
	v_cndmask_b32_e64 v18, v16, v46, s[4:5]
	v_cmp_lt_i32_e64 s[6:7], s6, v36
	v_lshl_or_b32 v12, v12, 6, v35
	v_lshl_or_b32 v15, v15, 6, v35
	s_waitcnt lgkmcnt(0)
	v_cndmask_b32_e64 v28, v16, v48, s[6:7]
	global_load_dwordx4 v[20:23], v12, s[20:21]
	global_load_dwordx4 v[24:27], v15, s[20:21]
	v_lshl_or_b32 v12, v18, 6, v35
	v_lshl_or_b32 v15, v28, 6, v35
	global_load_dwordx4 v[28:31], v12, s[20:21]
	global_load_dwordx4 v[40:43], v15, s[20:21]
	v_cndmask_b32_e32 v12, 0, v13, vcc
	v_cndmask_b32_e64 v13, 0, v45, s[0:1]
	v_cndmask_b32_e64 v15, 0, v47, s[4:5]
	v_cndmask_b32_e64 v18, 0, v49, s[6:7]
	s_waitcnt vmcnt(3)
	v_fma_mix_f32 v2, v20, v12, v2 op_sel:[0,0,0] op_sel_hi:[1,0,0]
	v_fma_mix_f32 v3, v20, v12, v3 op_sel:[1,0,0] op_sel_hi:[1,0,0]
	v_fma_mix_f32 v4, v21, v12, v4 op_sel:[0,0,0] op_sel_hi:[1,0,0]
	v_fma_mix_f32 v5, v21, v12, v5 op_sel:[1,0,0] op_sel_hi:[1,0,0]
	v_fma_mix_f32 v6, v22, v12, v6 op_sel:[0,0,0] op_sel_hi:[1,0,0]
	v_fma_mix_f32 v7, v22, v12, v7 op_sel:[1,0,0] op_sel_hi:[1,0,0]
	v_fma_mix_f32 v8, v23, v12, v8 op_sel:[0,0,0] op_sel_hi:[1,0,0]
	v_fma_mix_f32 v9, v23, v12, v9 op_sel:[1,0,0] op_sel_hi:[1,0,0]
	v_add_f32_e32 v12, v38, v12
	v_add_f32_e32 v12, v12, v13
	s_add_i32 s26, s26, 4
	s_waitcnt vmcnt(2)
	v_fma_mix_f32 v2, v24, v13, v2 op_sel:[0,0,0] op_sel_hi:[1,0,0]
	v_fma_mix_f32 v3, v24, v13, v3 op_sel:[1,0,0] op_sel_hi:[1,0,0]
	v_fma_mix_f32 v4, v25, v13, v4 op_sel:[0,0,0] op_sel_hi:[1,0,0]
	v_fma_mix_f32 v5, v25, v13, v5 op_sel:[1,0,0] op_sel_hi:[1,0,0]
	v_fma_mix_f32 v6, v26, v13, v6 op_sel:[0,0,0] op_sel_hi:[1,0,0]
	v_fma_mix_f32 v7, v26, v13, v7 op_sel:[1,0,0] op_sel_hi:[1,0,0]
	v_fma_mix_f32 v8, v27, v13, v8 op_sel:[0,0,0] op_sel_hi:[1,0,0]
	v_fma_mix_f32 v9, v27, v13, v9 op_sel:[1,0,0] op_sel_hi:[1,0,0]
	v_add_f32_e32 v12, v12, v15
	v_cmp_ge_i32_e32 vcc, s26, v10
	s_waitcnt vmcnt(1)
	v_fma_mix_f32 v2, v28, v15, v2 op_sel:[0,0,0] op_sel_hi:[1,0,0]
	v_fma_mix_f32 v3, v28, v15, v3 op_sel:[1,0,0] op_sel_hi:[1,0,0]
	v_fma_mix_f32 v4, v29, v15, v4 op_sel:[0,0,0] op_sel_hi:[1,0,0]
	v_fma_mix_f32 v5, v29, v15, v5 op_sel:[1,0,0] op_sel_hi:[1,0,0]
	v_fma_mix_f32 v6, v30, v15, v6 op_sel:[0,0,0] op_sel_hi:[1,0,0]
	v_fma_mix_f32 v7, v30, v15, v7 op_sel:[1,0,0] op_sel_hi:[1,0,0]
	v_fma_mix_f32 v8, v31, v15, v8 op_sel:[0,0,0] op_sel_hi:[1,0,0]
	v_fma_mix_f32 v9, v31, v15, v9 op_sel:[1,0,0] op_sel_hi:[1,0,0]
	s_or_b64 s[24:25], vcc, s[24:25]
	v_add_f32_e32 v38, v12, v18
	s_waitcnt vmcnt(0)
	v_fma_mix_f32 v2, v40, v18, v2 op_sel:[0,0,0] op_sel_hi:[1,0,0]
	v_fma_mix_f32 v3, v40, v18, v3 op_sel:[1,0,0] op_sel_hi:[1,0,0]
	v_fma_mix_f32 v4, v41, v18, v4 op_sel:[0,0,0] op_sel_hi:[1,0,0]
	v_fma_mix_f32 v5, v41, v18, v5 op_sel:[1,0,0] op_sel_hi:[1,0,0]
	v_fma_mix_f32 v6, v42, v18, v6 op_sel:[0,0,0] op_sel_hi:[1,0,0]
	v_fma_mix_f32 v7, v42, v18, v7 op_sel:[1,0,0] op_sel_hi:[1,0,0]
	v_fma_mix_f32 v8, v43, v18, v8 op_sel:[0,0,0] op_sel_hi:[1,0,0]
	v_fma_mix_f32 v9, v43, v18, v9 op_sel:[1,0,0] op_sel_hi:[1,0,0]
	s_andn2_b64 exec, exec, s[24:25]
	s_cbranch_execnz .LBB4_24
	s_or_b64 exec, exec, s[24:25]
